# v13 + MoBA-C: list counts in LDS, stale waits removed, result stores drain behind the next item fetch + seam-6 arrive without L2 write-back + write-through stores for the phase-4 weight images
# speedup vs baseline: 1.0034x; 1.0033x over previous
.LBB0_1375:
	s_or_b64 exec, exec, s[24:25]
	s_branch .Lmc_bottom

.Lmc_bottom:
	v_mov_b64_e32 v[82:83], v[142:143]
	v_mov_b64_e32 v[86:87], v[138:139]
	v_mov_b64_e32 v[90:91], v[134:135]
	v_mov_b64_e32 v[94:95], v[130:131]
	v_mov_b64_e32 v[98:99], v[126:127]
	v_mov_b64_e32 v[102:103], v[122:123]
	v_mov_b64_e32 v[106:107], v[118:119]
	v_mov_b64_e32 v[110:111], v[114:115]
	s_andn2_b64 vcc, exec, s[18:19]
	v_mov_b64_e32 v[84:85], v[144:145]
	v_mov_b64_e32 v[88:89], v[140:141]
	v_mov_b64_e32 v[92:93], v[136:137]
	v_mov_b64_e32 v[96:97], v[132:133]
	v_mov_b64_e32 v[100:101], v[128:129]
	v_mov_b64_e32 v[104:105], v[124:125]
	v_mov_b64_e32 v[108:109], v[120:121]
	v_mov_b64_e32 v[112:113], v[116:117]
	s_mov_b64 s[14:15], s[20:21]
	s_mov_b64 s[24:25], s[22:23]
	v_mov_b32_e32 v155, v151
	v_mov_b32_e32 v148, v153
	s_cbranch_vccz .LBB0_1393

.LBB0_1383:
	s_add_i32 s20, s10, s11
	s_add_i32 s20, s20, 1
	s_ashr_i32 s20, s20, 1
	s_lshl_b32 s21, s20, 2
	s_add_i32 s21, s21, 0
	s_add_i32 s21, s21, 0x21000
	v_mov_b32_e32 v2, s21
	ds_read_b32 v2, v2
	s_add_i32 s21, s20, -1
	s_waitcnt lgkmcnt(0)
	v_readfirstlane_b32 s22, v2
	s_cmp_gt_i32 s22, s6
	s_cselect_b32 s11, s21, s11
	s_cselect_b32 s10, s10, s20
	s_cmp_lt_i32 s10, s11
	s_cbranch_scc1 .LBB0_1383
	s_lshl_b32 s11, s10, 2
	s_add_i32 s11, s11, 0
	s_add_i32 s11, s11, 0x21000
	v_mov_b32_e32 v2, s11
	s_ashr_i32 s11, s10, 31
	s_lshl_b64 s[20:21], s[10:11], 2
	s_add_u32 s20, s7, s20
	s_addc_u32 s21, s9, s21
	v_mov_b32_e32 v151, 0
	ds_read_b32 v3, v2
	ds_read_b32 v2, v2 offset:2048
	v_mov_b64_e32 v[116:117], v[112:113]
	v_mov_b64_e32 v[120:121], v[108:109]
	v_mov_b64_e32 v[124:125], v[104:105]
	s_waitcnt lgkmcnt(0)
	v_sub_u32_e32 v3, s6, v3
	v_lshlrev_b32_e32 v3, 8, v3
	v_add_u32_e32 v3, s26, v3
	v_mov_b64_e32 v[128:129], v[100:101]
	v_mov_b64_e32 v[132:133], v[96:97]
	v_mov_b64_e32 v[136:137], v[92:93]
	v_mov_b64_e32 v[140:141], v[88:89]
	v_mov_b64_e32 v[144:145], v[84:85]
	s_mov_b64 s[20:21], 0
	s_mov_b64 s[22:23], 0
	v_mov_b32_e32 v153, 0
	v_mov_b64_e32 v[114:115], v[110:111]
	v_mov_b64_e32 v[118:119], v[106:107]
	v_mov_b64_e32 v[122:123], v[102:103]
	v_mov_b64_e32 v[126:127], v[98:99]
	v_mov_b64_e32 v[130:131], v[94:95]
	v_mov_b64_e32 v[134:135], v[90:91]
	v_mov_b64_e32 v[138:139], v[86:87]
	v_mov_b64_e32 v[142:143], v[82:83]
	v_cmp_ge_i32_e32 vcc, v3, v2
	s_cbranch_vccnz .LBB0_1387
	s_and_b32 s11, s10, 63
	s_add_i32 s23, s11, -1
	s_mul_i32 s22, s11, 63
	s_mul_i32 s11, s23, s11
	s_lshr_b32 s23, s11, 31
	s_add_i32 s11, s11, s23
	s_sext_i32_i16 s11, s11
	s_lshr_b32 s11, s11, 1
	s_sub_i32 s11, 0, s11
	s_sext_i32_i16 s11, s11
	s_ashr_i32 s20, s10, 6
	v_or_b32_e32 v4, v3, v156
	s_add_i32 s22, s22, s11
	s_mul_i32 s21, s20, 0x7e000
	s_lshl_b32 s11, s22, 8
	v_cmp_lt_i32_e32 vcc, v4, v2
	s_add_i32 s11, s11, s21
	s_ashr_i32 s21, s20, 31
	v_cndmask_b32_e32 v2, v3, v4, vcc
	v_add_u32_e32 v2, s11, v2
	v_ashrrev_i32_e32 v3, 31, v2
	v_lshl_add_u64 v[2:3], v[2:3], 2, s[12:13]
	global_load_dword v4, v[2:3], off
	s_lshl_b64 s[20:21], s[20:21], 22
	s_add_u32 s20, s27, s20
	v_mov_b32_e32 v3, v149
	s_addc_u32 s21, s28, s21
	s_mov_b64 s[22:23], -1
	s_waitcnt vmcnt(0)
	v_and_b32_e32 v153, 0xffff, v4
	v_lshlrev_b32_e32 v2, 8, v153
	v_lshl_add_u64 v[2:3], s[20:21], 0, v[2:3]
	v_lshl_add_u64 v[2:3], v[146:147], 1, v[2:3]
	global_load_dwordx4 v[114:117], v[2:3], off
	global_load_dwordx4 v[118:121], v[2:3], off offset:32
	global_load_dwordx4 v[122:125], v[2:3], off offset:64
	global_load_dwordx4 v[126:129], v[2:3], off offset:96
	global_load_dwordx4 v[130:133], v[2:3], off offset:128
	global_load_dwordx4 v[134:137], v[2:3], off offset:160
	global_load_dwordx4 v[138:141], v[2:3], off offset:192
	global_load_dwordx4 v[142:145], v[2:3], off offset:224
	v_lshrrev_b32_e32 v151, 16, v4
	s_and_b64 s[20:21], vcc, exec
	s_branch .LBB0_1387

.LBB0_1389:
	v_add_u32_e32 v166, 0, v194
	s_waitcnt lgkmcnt(0)
	ds_read_b128 v[66:69], v166
	ds_read_b128 v[204:207], v166 offset:32
	v_add_u32_e32 v203, 0, v195
	v_add_u32_e32 v217, 0, v197
	v_add_u32_e32 v218, 0, v198
	s_waitcnt lgkmcnt(1)
	v_mfma_f32_32x32x16_bf16 v[66:81], v[66:69], v[110:113], 0
	v_add_u32_e32 v216, 0, v196
	v_add_u32_e32 v219, 0x11800, v216
	v_add_u32_e32 v220, 0, v199
	v_add_u32_e32 v221, 0, v200
	v_add_u32_e32 v222, 0, v201
	v_add_u32_e32 v223, 0, v202
	v_add_u32_e32 v224, 0x11000, v220
	s_waitcnt lgkmcnt(0)
	v_mfma_f32_32x32x16_bf16 v[66:81], v[204:207], v[106:109], v[66:81]
	ds_read_b128 v[204:207], v166 offset:64
	ds_read_b128 v[208:211], v166 offset:96
	v_add_u32_e32 v216, 0x12800, v216
	v_add_u32_e32 v225, 0x11800, v221
	v_add_u32_e32 v226, 0x11000, v222
	v_add_u32_e32 v227, 0x11800, v223
	s_add_i32 s11, s11, -1
	v_add_u32_e32 v202, 0x2000, v202
	s_waitcnt lgkmcnt(1)
	v_mfma_f32_32x32x16_bf16 v[66:81], v[204:207], v[102:105], v[66:81]
	v_add_u32_e32 v201, 0x2000, v201
	v_add_u32_e32 v200, 0x2000, v200
	v_add_u32_e32 v199, 0x2000, v199
	v_add_u32_e32 v198, 0x2000, v198
	v_add_u32_e32 v197, 0x2000, v197
	v_add_u32_e32 v196, 0x2000, v196
	v_add_u32_e32 v195, 0x2000, v195
	s_waitcnt lgkmcnt(0)
	v_mfma_f32_32x32x16_bf16 v[66:81], v[208:211], v[98:101], v[66:81]
	ds_read_b128 v[204:207], v166 offset:128
	ds_read_b128 v[208:211], v166 offset:160
	v_add_u32_e32 v194, 0x2200, v194
	s_cmp_lg_u32 s11, 0
	s_waitcnt lgkmcnt(1)
	v_mfma_f32_32x32x16_bf16 v[66:81], v[204:207], v[94:97], v[66:81]
	ds_read_b128 v[204:207], v166 offset:192
	ds_read_b128 v[212:215], v166 offset:224
	v_add_u32_e32 v166, 0x11000, v203
	v_add_u32_e32 v203, 0x12000, v203
	s_waitcnt lgkmcnt(2)
	v_mfma_f32_32x32x16_bf16 v[66:81], v[208:211], v[90:93], v[66:81]
	v_add_u32_e32 v208, 0x11000, v217
	v_add_u32_e32 v210, 0x11800, v218
	v_add_u32_e32 v217, 0x12000, v217
	v_add_u32_e32 v218, 0x12800, v218
	s_waitcnt lgkmcnt(1)
	v_mfma_f32_32x32x16_bf16 v[66:81], v[204:207], v[86:89], v[66:81]
	ds_read_b64_tr_b16 v[204:205], v166
	ds_read_b64_tr_b16 v[206:207], v219
	ds_read_b64_tr_b16 v[208:209], v208
	ds_read_b64_tr_b16 v[210:211], v210
	s_waitcnt lgkmcnt(4)
	v_mfma_f32_32x32x16_bf16 v[66:81], v[212:215], v[82:85], v[66:81]
	s_nop 11
	v_fma_f32 v66, v66, s29, -v158
	v_fma_f32 v67, v67, s29, -v158
	v_fma_f32 v68, v68, s29, -v158
	v_fma_f32 v69, v69, s29, -v158
	v_fma_f32 v70, v70, s29, -v158
	v_fma_f32 v71, v71, s29, -v158
	v_fma_f32 v72, v72, s29, -v158
	v_fma_f32 v73, v73, s29, -v158
	v_exp_f32_e32 v166, v66
	v_exp_f32_e32 v228, v67
	v_exp_f32_e32 v229, v68
	v_exp_f32_e32 v230, v69
	v_exp_f32_e32 v231, v70
	v_exp_f32_e32 v232, v71
	v_exp_f32_e32 v233, v72
	v_exp_f32_e32 v234, v73
	v_cvt_pk_bf16_f32 v66, v166, v228
	v_cvt_pk_bf16_f32 v67, v229, v230
	v_cvt_pk_bf16_f32 v68, v231, v232
	v_cvt_pk_bf16_f32 v69, v233, v234
	v_fma_f32 v74, v74, s29, -v158
	v_fma_f32 v75, v75, s29, -v158
	s_waitcnt lgkmcnt(2)
	v_mfma_f32_32x32x16_bf16 v[50:65], v[204:207], v[66:69], v[50:65]
	ds_read_b64_tr_b16 v[70:71], v224
	ds_read_b64_tr_b16 v[72:73], v225
	ds_read_b64_tr_b16 v[204:205], v226
	ds_read_b64_tr_b16 v[206:207], v227
	ds_read_b64_tr_b16 v[212:213], v203
	ds_read_b64_tr_b16 v[214:215], v216
	ds_read_b64_tr_b16 v[216:217], v217
	ds_read_b64_tr_b16 v[218:219], v218
	v_fma_f32 v76, v76, s29, -v158
	v_fma_f32 v77, v77, s29, -v158
	v_fma_f32 v78, v78, s29, -v158
	v_fma_f32 v79, v79, s29, -v158
	v_exp_f32_e32 v203, v76
	s_waitcnt lgkmcnt(6)
	v_mfma_f32_32x32x16_bf16 v[18:33], v[70:73], v[66:69], v[18:33]
	v_fma_f32 v70, v80, s29, -v158
	v_fma_f32 v71, v81, s29, -v158
	v_exp_f32_e32 v80, v74
	v_exp_f32_e32 v81, v75
	v_exp_f32_e32 v78, v78
	v_exp_f32_e32 v79, v79
	v_add_u32_e32 v72, 0x12800, v221
	s_waitcnt lgkmcnt(4)
	v_mfma_f32_32x32x16_bf16 v[2:17], v[204:207], v[66:69], v[2:17]
	v_exp_f32_e32 v204, v70
	v_add_u32_e32 v70, 0x12000, v220
	v_exp_f32_e32 v205, v71
	ds_read_b64_tr_b16 v[70:71], v70
	v_add_u32_e32 v74, 0x12000, v222
	v_add_u32_e32 v76, 0x12800, v223
	v_add_f32_e32 v166, v193, v166
	v_mfma_f32_32x32x16_bf16 v[34:49], v[208:211], v[66:69], v[34:49]
	v_exp_f32_e32 v208, v77
	ds_read_b64_tr_b16 v[72:73], v72
	ds_read_b64_tr_b16 v[74:75], v74
	ds_read_b64_tr_b16 v[76:77], v76
	v_cvt_pk_bf16_f32 v66, v80, v81
	v_cvt_pk_bf16_f32 v68, v78, v79
	v_cvt_pk_bf16_f32 v67, v203, v208
	v_cvt_pk_bf16_f32 v69, v204, v205
	v_add_f32_e32 v166, v228, v166
	s_waitcnt lgkmcnt(2)
	v_mfma_f32_32x32x16_bf16 v[18:33], v[70:73], v[66:69], v[18:33]
	v_add_f32_e32 v70, v229, v166
	v_add_f32_e32 v70, v230, v70
	v_add_f32_e32 v70, v231, v70
	v_add_f32_e32 v70, v232, v70
	v_add_f32_e32 v70, v233, v70
	v_add_f32_e32 v70, v234, v70
	v_add_f32_e32 v70, v80, v70
	v_mfma_f32_32x32x16_bf16 v[50:65], v[212:215], v[66:69], v[50:65]
	v_mfma_f32_32x32x16_bf16 v[34:49], v[216:219], v[66:69], v[34:49]
	s_waitcnt lgkmcnt(0)
	v_mfma_f32_32x32x16_bf16 v[2:17], v[74:77], v[66:69], v[2:17]
	v_add_f32_e32 v66, v81, v70
	v_add_f32_e32 v66, v203, v66
	v_add_f32_e32 v66, v208, v66
	v_add_f32_e32 v66, v78, v66
	v_add_f32_e32 v66, v79, v66
	v_add_f32_e32 v66, v204, v66
	v_add_f32_e32 v193, v205, v66
	s_cbranch_scc1 .LBB0_1389
	s_waitcnt vmcnt(0)
	ds_bpermute_b32 v68, v1, v193
	s_and_saveexec_b64 s[24:25], s[14:15]
	s_cbranch_execz .LBB0_1375
	v_lshl_add_u32 v66, v155, 2, s16
	v_ashrrev_i32_e32 v67, 31, v66
	v_lshlrev_b64 v[70:71], 22, v[66:67]
	v_lshl_add_u64 v[70:71], s[44:45], 0, v[70:71]
	v_lshlrev_b64 v[72:73], 8, v[148:149]
	v_lshl_add_u64 v[70:71], v[70:71], 0, v[72:73]
	v_mov_b32_e32 v155, v149
	v_lshl_add_u64 v[70:71], v[70:71], 0, v[154:155]
	v_cvt_pk_bf16_f32 v50, v50, v51
	v_cvt_pk_bf16_f32 v51, v52, v53
	v_cvt_pk_bf16_f32 v52, v54, v55
	v_cvt_pk_bf16_f32 v53, v56, v57
	v_cvt_pk_bf16_f32 v34, v34, v35
	v_cvt_pk_bf16_f32 v35, v36, v37
	v_cvt_pk_bf16_f32 v36, v38, v39
	v_cvt_pk_bf16_f32 v37, v40, v41
	v_cvt_pk_bf16_f32 v18, v18, v19
	v_cvt_pk_bf16_f32 v19, v20, v21
	v_cvt_pk_bf16_f32 v20, v22, v23
	v_cvt_pk_bf16_f32 v21, v24, v25
	v_cvt_pk_bf16_f32 v2, v2, v3
	v_cvt_pk_bf16_f32 v3, v4, v5
	v_cvt_pk_bf16_f32 v4, v6, v7
	v_cvt_pk_bf16_f32 v5, v8, v9
	global_store_dwordx4 v[70:71], v[50:53], off
	global_store_dwordx4 v[70:71], v[34:37], off offset:32
	global_store_dwordx4 v[70:71], v[18:21], off offset:64
	v_cvt_pk_bf16_f32 v50, v58, v59
	v_cvt_pk_bf16_f32 v51, v60, v61
	v_cvt_pk_bf16_f32 v52, v62, v63
	v_cvt_pk_bf16_f32 v53, v64, v65
	v_cvt_pk_bf16_f32 v34, v42, v43
	v_cvt_pk_bf16_f32 v35, v44, v45
	v_cvt_pk_bf16_f32 v36, v46, v47
	v_cvt_pk_bf16_f32 v37, v48, v49
	v_cvt_pk_bf16_f32 v18, v26, v27
	v_cvt_pk_bf16_f32 v19, v28, v29
	v_cvt_pk_bf16_f32 v20, v30, v31
	v_cvt_pk_bf16_f32 v21, v32, v33
	global_store_dwordx4 v[70:71], v[2:5], off offset:96
	global_store_dwordx4 v[70:71], v[50:53], off offset:16
	global_store_dwordx4 v[70:71], v[34:37], off offset:48
	v_cvt_pk_bf16_f32 v2, v10, v11
	v_cvt_pk_bf16_f32 v3, v12, v13
	v_cvt_pk_bf16_f32 v4, v14, v15
	v_cvt_pk_bf16_f32 v5, v16, v17
	global_store_dwordx4 v[70:71], v[18:21], off offset:80
	global_store_dwordx4 v[70:71], v[2:5], off offset:112
	s_and_b64 exec, exec, s[4:5]
	s_cbranch_execz .LBB0_1375
	v_lshlrev_b64 v[2:3], 16, v[66:67]
	v_lshl_add_u64 v[2:3], s[0:1], 0, v[2:3]
	s_waitcnt lgkmcnt(0)
	v_add_f32_e32 v4, v193, v68
	v_lshl_add_u64 v[2:3], v[148:149], 2, v[2:3]
	global_store_dword v[2:3], v4, off
	s_branch .LBB0_1375
